# prologue transposes: s_barrier per item so the 8 waves of a workgroup load adjacent column blocks of the same rows together
# speedup vs baseline: 1.0132x; 1.0132x over previous
.LBB0_78:
	s_barrier
	s_abs_i32 s41, s39
	s_mul_hi_u32 s42, s41, s3
	s_mul_i32 s43, s42, s4
	s_sub_i32 s41, s41, s43
	s_ashr_i32 s40, s39, 31
	s_add_i32 s43, s42, 1
	s_sub_i32 s86, s41, s4
	s_cmp_ge_u32 s41, s4
	s_cselect_b32 s42, s43, s42
	s_cselect_b32 s41, s86, s41
	s_add_i32 s43, s42, 1
	s_cmp_ge_u32 s41, s4
	s_cselect_b32 s41, s43, s42
	s_xor_b32 s41, s41, s40
	s_sub_i32 s41, s41, s40
	s_lshl_b32 s86, s41, 6
	s_mul_i32 s40, s51, s41
	v_or_b32_e32 v1, s86, v75
	s_ashr_i32 s87, s86, 31
	s_add_i32 s40, s40, s38
	s_mul_i32 s42, s87, s10
	v_mad_u64_u32 v[2:3], s[88:89], v1, s10, 0
	v_add_u32_e32 v0, s40, v74
	v_add_u32_e32 v3, s42, v3
	s_waitcnt lgkmcnt(0)
	v_lshl_add_u64 v[2:3], v[2:3], 2, s[52:53]
	v_ashrrev_i32_e32 v1, 31, v0
	v_cmp_gt_i32_e32 vcc, s10, v0
	v_lshl_add_u64 v[68:69], v[0:1], 2, v[2:3]
	v_mov_b32_e32 v4, 0
	v_mov_b32_e32 v0, 0
	v_mov_b32_e32 v1, 0
	v_mov_b32_e32 v2, 0
	v_mov_b32_e32 v3, 0
	s_and_saveexec_b64 s[88:89], vcc
	s_cbranch_execz .LBB0_80
	global_load_dwordx4 v[0:3], v[68:69], off nt

.LBB0_117:
	s_barrier
	s_abs_i32 s3, s33
	s_mul_hi_u32 s38, s3, s67
	s_mul_i32 s39, s38, s4
	s_sub_i32 s3, s3, s39
	s_ashr_i32 s2, s33, 31
	s_add_i32 s39, s38, 1
	s_sub_i32 s40, s3, s4
	s_cmp_ge_u32 s3, s4
	s_cselect_b32 s38, s39, s38
	s_cselect_b32 s3, s40, s3
	s_add_i32 s39, s38, 1
	s_cmp_ge_u32 s3, s4
	s_cselect_b32 s3, s39, s38
	s_xor_b32 s3, s3, s2
	s_sub_i32 s70, s3, s2
	s_mul_i32 s2, s64, s70
	s_add_i32 s71, s33, s2
	s_mul_i32 s2, s66, s70
	s_lshl_b32 s60, s70, 7
	s_add_i32 s69, s68, s2
	v_add_u32_e32 v0, s69, v74
	s_cmpk_lt_i32 s71, 0x58
	s_cselect_b64 s[62:63], -1, 0
	v_or_b32_e32 v48, s60, v76
	v_ashrrev_i32_e32 v1, 31, v0
	s_ashr_i32 s61, s60, 31
	s_waitcnt lgkmcnt(0)
	v_lshl_add_u64 v[36:37], v[0:1], 2, s[52:53]
	s_mul_i32 s2, s61, s10
	v_mad_u64_u32 v[0:1], s[38:39], v48, s10, 0
	v_add_u32_e32 v1, s2, v1
	v_lshl_add_u64 v[0:1], v[0:1], 2, v[36:37]
	global_load_dwordx4 v[24:27], v[0:1], off nt
	v_lshl_add_u64 v[0:1], v[0:1], 0, s[0:1]
	global_load_dwordx4 v[32:35], v[0:1], off nt
	v_lshl_add_u64 v[0:1], v[0:1], 0, s[0:1]
	global_load_dwordx4 v[40:43], v[0:1], off nt
	v_lshl_add_u64 v[0:1], v[0:1], 0, s[0:1]
	global_load_dwordx4 v[44:47], v[0:1], off nt
	v_lshl_add_u64 v[0:1], v[0:1], 0, s[58:59]
	v_lshl_add_u64 v[2:3], v[0:1], 0, s[0:1]
	global_load_dwordx4 v[12:15], v[0:1], off nt
	global_load_dwordx4 v[8:11], v[2:3], off nt
	v_lshl_add_u64 v[0:1], v[2:3], 0, s[0:1]
	v_lshl_add_u64 v[16:17], v[0:1], 0, s[0:1]
	global_load_dwordx4 v[4:7], v[0:1], off nt
	s_nop 0
	global_load_dwordx4 v[0:3], v[16:17], off nt
	v_lshl_add_u64 v[16:17], v[16:17], 0, s[58:59]
	v_lshl_add_u64 v[20:21], v[16:17], 0, s[0:1]
	s_and_b64 vcc, s[56:57], s[62:63]
	global_load_dwordx4 v[28:31], v[16:17], off nt
	v_cndmask_b32_e32 v52, v89, v50, vcc
	global_load_dwordx4 v[16:19], v[20:21], off nt
	v_lshl_add_u64 v[38:39], v[20:21], 0, s[0:1]
	global_load_dwordx4 v[20:23], v[38:39], off nt
	v_lshl_add_u64 v[38:39], v[38:39], 0, s[0:1]
	v_mov_b32_e32 v53, 0
	v_mov_b32_e32 v68, 0
	v_mov_b32_e32 v69, 0
	v_mov_b32_e32 v90, 0
	v_mov_b32_e32 v54, 0
	v_mov_b32_e32 v91, 0
	v_add_u32_e32 v51, v77, v78
	s_andn2_b64 vcc, exec, s[56:57]
	s_waitcnt vmcnt(10)
	v_mul_f32_e32 v55, v24, v52
	v_mul_f32_e32 v56, v25, v52
	s_waitcnt vmcnt(9)
	v_mul_f32_e32 v59, v32, v52
	v_or_b32_e32 v32, 64, v48
	v_mul_f32_e32 v60, v33, v52
	v_mad_u64_u32 v[32:33], s[38:39], v32, s10, 0
	v_add_u32_e32 v33, s2, v33
	v_mul_f32_e32 v57, v26, v52
	v_mul_f32_e32 v58, v27, v52
	global_load_dwordx4 v[24:27], v[38:39], off nt
	v_lshl_add_u64 v[48:49], v[32:33], 2, v[36:37]
	v_lshl_add_u64 v[32:33], v[38:39], 0, s[58:59]
	v_mul_f32_e32 v34, v34, v52
	v_cvt_pk_fp8_f32 v53, v55, v59
	global_load_dwordx4 v[36:39], v[32:33], off nt
	v_lshl_add_u64 v[32:33], v[32:33], 0, s[0:1]
	v_cvt_pk_fp8_f32 v68, v56, v60
	v_cvt_pk_fp8_f32 v69, v57, v34
	s_waitcnt vmcnt(9)
	v_mul_f32_e32 v34, v52, v44
	v_mul_f32_e32 v59, v52, v45
	v_mul_f32_e32 v60, v52, v46
	v_mul_f32_e32 v61, v52, v47
	global_load_dwordx4 v[44:47], v[32:33], off nt
	v_mul_f32_e32 v40, v40, v52
	v_lshl_add_u64 v[32:33], v[32:33], 0, s[0:1]
	v_mul_f32_e32 v35, v35, v52
	v_mul_f32_e32 v55, v41, v52
	v_mul_f32_e32 v56, v42, v52
	v_mul_f32_e32 v57, v43, v52
	v_cvt_pk_fp8_f32 v53, v40, v34 op_sel:[0,0,1]
	global_load_dwordx4 v[40:43], v[32:33], off nt
	v_lshl_add_u64 v[32:33], v[32:33], 0, s[0:1]
	v_cvt_pk_fp8_f32 v90, v58, v35
	global_load_dwordx4 v[32:35], v[32:33], off nt
	s_waitcnt vmcnt(11)
	v_mul_f32_e32 v12, v52, v12
	s_waitcnt vmcnt(10)
	v_mul_f32_e32 v8, v52, v8
	v_cvt_pk_fp8_f32 v54, v12, v8
	s_waitcnt vmcnt(9)
	v_mul_f32_e32 v4, v52, v4
	s_waitcnt vmcnt(8)
	v_mul_f32_e32 v0, v52, v0
	v_mov_b32_e32 v8, 0
	v_cvt_pk_fp8_f32 v54, v4, v0 op_sel:[0,0,1]
	v_mul_f32_e32 v0, v52, v13
	v_mul_f32_e32 v4, v52, v9
	v_cvt_pk_fp8_f32 v91, v0, v4
	v_mul_f32_e32 v0, v52, v14
	v_mul_f32_e32 v4, v52, v5
	v_mul_f32_e32 v5, v52, v10
	v_cvt_pk_fp8_f32 v8, v0, v5
	v_mul_f32_e32 v0, v52, v1
	v_cvt_pk_fp8_f32 v91, v4, v0 op_sel:[0,0,1]
	v_mul_f32_e32 v0, v52, v6
	v_mul_f32_e32 v1, v52, v2
	v_cvt_pk_fp8_f32 v68, v55, v59 op_sel:[0,0,1]
	v_cvt_pk_fp8_f32 v69, v56, v60 op_sel:[0,0,1]
	ds_write2_b32 v51, v53, v54 offset1:4
	v_cvt_pk_fp8_f32 v8, v0, v1 op_sel:[0,0,1]
	v_lshl_add_u64 v[62:63], v[48:49], 0, s[0:1]
	v_cvt_pk_fp8_f32 v90, v57, v61 op_sel:[0,0,1]
	global_load_dwordx4 v[54:57], v[48:49], off nt
	global_load_dwordx4 v[58:61], v[62:63], off nt
	v_lshl_add_u64 v[0:1], v[62:63], 0, s[0:1]
	ds_write2_b32 v51, v68, v91 offset0:33 offset1:37
	ds_write2_b32 v51, v69, v8 offset0:66 offset1:70
	v_mul_f32_e32 v2, v52, v15
	v_lshl_add_u64 v[4:5], v[0:1], 0, s[0:1]
	v_mul_f32_e32 v6, v52, v11
	global_load_dwordx4 v[8:11], v[0:1], off nt
	global_load_dwordx4 v[12:15], v[4:5], off nt
	v_mov_b32_e32 v53, 0
	v_cvt_pk_fp8_f32 v53, v2, v6
	v_mul_f32_e32 v2, v52, v7
	v_mul_f32_e32 v3, v52, v3
	v_lshl_add_u64 v[0:1], v[4:5], 0, s[58:59]
	v_cvt_pk_fp8_f32 v53, v2, v3 op_sel:[0,0,1]
	v_lshl_add_u64 v[48:49], v[0:1], 0, s[0:1]
	s_waitcnt vmcnt(11)
	v_mul_f32_e32 v2, v52, v28
	s_waitcnt vmcnt(10)
	v_mul_f32_e32 v3, v52, v16
	v_mov_b32_e32 v62, 0
	v_cvt_pk_fp8_f32 v62, v2, v3
	v_mul_f32_e32 v16, v52, v29
	global_load_dwordx4 v[0:3], v[0:1], off nt
	s_nop 0
	global_load_dwordx4 v[4:7], v[48:49], off nt
	v_lshl_add_u64 v[28:29], v[48:49], 0, s[0:1]
	v_mul_f32_e32 v17, v52, v17
	v_mov_b32_e32 v48, 0
	v_mul_f32_e32 v30, v52, v30
	ds_write2_b32 v51, v90, v53 offset0:99 offset1:103
	v_cvt_pk_fp8_f32 v48, v16, v17
	v_mul_f32_e32 v16, v52, v18
	v_mov_b32_e32 v53, 0
	v_cvt_pk_fp8_f32 v53, v30, v16
	s_waitcnt vmcnt(11)
	v_mul_f32_e32 v20, v52, v20
	s_waitcnt vmcnt(10)
	v_mul_f32_e32 v24, v52, v24
	v_mul_f32_e32 v16, v52, v21
	v_mul_f32_e32 v17, v52, v25
	v_mul_f32_e32 v31, v52, v31
	v_cvt_pk_fp8_f32 v62, v20, v24 op_sel:[0,0,1]
	v_cvt_pk_fp8_f32 v48, v16, v17 op_sel:[0,0,1]
	v_mul_f32_e32 v16, v52, v22
	v_mul_f32_e32 v17, v52, v26
	v_lshl_add_u64 v[24:25], v[28:29], 0, s[0:1]
	v_mul_f32_e32 v26, v52, v19
	v_mov_b32_e32 v63, 0
	v_cvt_pk_fp8_f32 v53, v16, v17 op_sel:[0,0,1]
	v_mul_f32_e32 v30, v52, v23
	global_load_dwordx4 v[16:19], v[28:29], off nt
	global_load_dwordx4 v[20:23], v[24:25], off nt
	v_lshl_add_u64 v[28:29], v[24:25], 0, s[58:59]
	v_mul_f32_e32 v24, v52, v27
	v_cvt_pk_fp8_f32 v63, v31, v26
	s_waitcnt vmcnt(11)
	v_mul_f32_e32 v25, v52, v36
	s_waitcnt vmcnt(10)
	v_mul_f32_e32 v26, v52, v44
	v_mov_b32_e32 v27, 0
	v_cvt_pk_fp8_f32 v27, v25, v26
	v_cvt_pk_fp8_f32 v63, v30, v24 op_sel:[0,0,1]
	s_waitcnt vmcnt(9)
	v_mul_f32_e32 v24, v52, v40
	v_mov_b32_e32 v36, 0
	s_waitcnt vmcnt(8)
	v_mul_f32_e32 v25, v52, v32
	v_cvt_pk_fp8_f32 v27, v24, v25 op_sel:[0,0,1]
	v_mul_f32_e32 v24, v52, v37
	v_mul_f32_e32 v25, v52, v45
	v_cvt_pk_fp8_f32 v36, v24, v25
	v_mul_f32_e32 v24, v52, v41
	v_mul_f32_e32 v25, v52, v33
	v_lshl_add_u64 v[32:33], v[28:29], 0, s[0:1]
	v_cvt_pk_fp8_f32 v36, v24, v25 op_sel:[0,0,1]
	v_mul_f32_e32 v24, v52, v38
	v_mul_f32_e32 v25, v52, v46
	v_mov_b32_e32 v46, 0
	v_cvt_pk_fp8_f32 v46, v24, v25
	ds_write2_b32 v51, v62, v27 offset0:8 offset1:12
	global_load_dwordx4 v[24:27], v[28:29], off nt
	ds_write2_b32 v51, v48, v36 offset0:41 offset1:45
	global_load_dwordx4 v[28:31], v[32:33], off nt
	v_mul_f32_e32 v36, v52, v42
	v_mul_f32_e32 v34, v52, v34
	v_cvt_pk_fp8_f32 v46, v36, v34 op_sel:[0,0,1]
	v_lshl_add_u64 v[32:33], v[32:33], 0, s[0:1]
	v_mul_f32_e32 v49, v52, v39
	global_load_dwordx4 v[36:39], v[32:33], off nt
	v_lshl_add_u64 v[32:33], v[32:33], 0, s[0:1]
	v_mul_f32_e32 v34, v52, v47
	v_lshl_add_u64 v[44:45], v[32:33], 0, s[58:59]
	v_mov_b32_e32 v68, 0
	v_mul_f32_e32 v47, v52, v43
	global_load_dwordx4 v[40:43], v[32:33], off nt
	v_mul_f32_e32 v62, v52, v35
	v_cvt_pk_fp8_f32 v68, v49, v34
	global_load_dwordx4 v[32:35], v[44:45], off nt
	v_lshl_add_u64 v[48:49], v[44:45], 0, s[0:1]
	ds_write2_b32 v51, v53, v46 offset0:74 offset1:78
	s_waitcnt vmcnt(12)
	v_mul_f32_e32 v44, v52, v54
	s_waitcnt vmcnt(11)
	v_mul_f32_e32 v45, v52, v58
	v_mov_b32_e32 v53, 0
	v_cvt_pk_fp8_f32 v53, v44, v45
	s_waitcnt vmcnt(10)
	v_mul_f32_e32 v8, v52, v8
	s_waitcnt vmcnt(9)
	v_mul_f32_e32 v12, v52, v12
	v_mul_f32_e32 v54, v52, v55
	v_cvt_pk_fp8_f32 v53, v8, v12 op_sel:[0,0,1]
	v_mul_f32_e32 v8, v52, v59
	v_mov_b32_e32 v12, 0
	v_cvt_pk_fp8_f32 v68, v47, v62 op_sel:[0,0,1]
	v_mul_f32_e32 v55, v52, v56
	v_cvt_pk_fp8_f32 v12, v54, v8
	v_mul_f32_e32 v8, v52, v60
	v_mov_b32_e32 v62, 0
	global_load_dwordx4 v[44:47], v[48:49], off nt
	v_cvt_pk_fp8_f32 v62, v55, v8
	v_mul_f32_e32 v8, v52, v9
	v_mul_f32_e32 v9, v52, v13
	v_lshl_add_u64 v[48:49], v[48:49], 0, s[0:1]
	v_cvt_pk_fp8_f32 v12, v8, v9 op_sel:[0,0,1]
	v_mul_f32_e32 v8, v52, v10
	v_mul_f32_e32 v9, v52, v14
	v_mul_f32_e32 v58, v52, v57
	v_cvt_pk_fp8_f32 v62, v8, v9 op_sel:[0,0,1]
	v_mul_f32_e32 v10, v52, v61
	v_lshl_add_u64 v[8:9], v[48:49], 0, s[0:1]
	v_mov_b32_e32 v13, 0
	global_load_dwordx4 v[54:57], v[48:49], off nt
	v_cvt_pk_fp8_f32 v13, v58, v10
	global_load_dwordx4 v[58:61], v[8:9], off nt
	s_waitcnt vmcnt(11)
	v_mul_f32_e32 v0, v52, v0
	s_waitcnt vmcnt(10)
	v_mul_f32_e32 v4, v52, v4
	v_mov_b32_e32 v10, 0
	v_cvt_pk_fp8_f32 v10, v0, v4
	v_mul_f32_e32 v0, v52, v1
	v_mul_f32_e32 v1, v52, v5
	v_mov_b32_e32 v4, 0
	v_cvt_pk_fp8_f32 v4, v0, v1
	s_waitcnt vmcnt(9)
	v_mul_f32_e32 v0, v52, v17
	s_waitcnt vmcnt(8)
	v_mul_f32_e32 v1, v52, v21
	v_mul_f32_e32 v8, v52, v11
	v_cvt_pk_fp8_f32 v4, v0, v1 op_sel:[0,0,1]
	v_mul_f32_e32 v0, v52, v2
	v_mul_f32_e32 v1, v52, v6
	v_mov_b32_e32 v6, 0
	v_mul_f32_e32 v9, v52, v15
	v_cvt_pk_fp8_f32 v6, v0, v1
	v_mul_f32_e32 v0, v52, v3
	v_mul_f32_e32 v1, v52, v7
	v_mov_b32_e32 v3, 0
	v_cvt_pk_fp8_f32 v13, v8, v9 op_sel:[0,0,1]
	v_mul_f32_e32 v8, v52, v16
	v_mul_f32_e32 v9, v52, v20
	v_cvt_pk_fp8_f32 v3, v0, v1
	v_cvt_pk_fp8_f32 v10, v8, v9 op_sel:[0,0,1]
	v_mul_f32_e32 v2, v52, v18
	v_mul_f32_e32 v5, v52, v22
	v_cvt_pk_fp8_f32 v6, v2, v5 op_sel:[0,0,1]
	v_mul_f32_e32 v0, v52, v19
	v_mul_f32_e32 v1, v52, v23
	v_cvt_pk_fp8_f32 v3, v0, v1 op_sel:[0,0,1]
	ds_write2_b32 v51, v63, v68 offset0:107 offset1:111
	ds_write2_b32 v51, v53, v10 offset0:16 offset1:20
	ds_write2_b32 v51, v12, v4 offset0:49 offset1:53
	ds_write2_b32 v51, v62, v6 offset0:82 offset1:86
	ds_write2_b32 v51, v13, v3 offset0:115 offset1:119
	s_waitcnt vmcnt(7)
	v_mul_f32_e32 v0, v52, v24
	s_waitcnt vmcnt(6)
	v_mul_f32_e32 v1, v52, v28
	v_mov_b32_e32 v4, 0
	v_cvt_pk_fp8_f32 v4, v0, v1
	v_mul_f32_e32 v0, v52, v25
	v_mul_f32_e32 v1, v52, v29
	v_mov_b32_e32 v5, 0
	v_cvt_pk_fp8_f32 v5, v0, v1
	s_waitcnt vmcnt(5)
	v_mul_f32_e32 v0, v52, v37
	v_mov_b32_e32 v6, 0
	s_waitcnt vmcnt(4)
	v_mul_f32_e32 v1, v52, v41
	v_cvt_pk_fp8_f32 v5, v0, v1 op_sel:[0,0,1]
	v_mul_f32_e32 v0, v52, v26
	v_mul_f32_e32 v1, v52, v30
	v_cvt_pk_fp8_f32 v6, v0, v1
	v_mul_f32_e32 v0, v52, v27
	v_mul_f32_e32 v1, v52, v31
	v_mov_b32_e32 v7, 0
	v_cvt_pk_fp8_f32 v7, v0, v1
	v_mul_f32_e32 v0, v52, v39
	v_mul_f32_e32 v1, v52, v43
	v_mov_b32_e32 v8, 0
	v_cvt_pk_fp8_f32 v7, v0, v1 op_sel:[0,0,1]
	s_waitcnt vmcnt(3)
	v_mul_f32_e32 v0, v52, v32
	v_mov_b32_e32 v9, 0
	v_mul_f32_e32 v2, v52, v36
	v_mul_f32_e32 v3, v52, v40
	v_mov_b32_e32 v10, 0
	v_cvt_pk_fp8_f32 v4, v2, v3 op_sel:[0,0,1]
	v_mul_f32_e32 v2, v52, v38
	v_mul_f32_e32 v3, v52, v42
	s_waitcnt vmcnt(2)
	v_mul_f32_e32 v1, v52, v44
	v_cvt_pk_fp8_f32 v8, v0, v1
	v_mul_f32_e32 v0, v52, v33
	v_mul_f32_e32 v1, v52, v45
	v_cvt_pk_fp8_f32 v9, v0, v1
	v_mov_b32_e32 v11, 0
	v_cvt_pk_fp8_f32 v6, v2, v3 op_sel:[0,0,1]
	s_waitcnt vmcnt(1)
	v_mul_f32_e32 v0, v52, v55
	v_mul_f32_e32 v2, v52, v54
	s_waitcnt vmcnt(0)
	v_mul_f32_e32 v1, v52, v59
	v_cvt_pk_fp8_f32 v9, v0, v1 op_sel:[0,0,1]
	v_mul_f32_e32 v0, v52, v34
	v_mul_f32_e32 v1, v52, v46
	v_cvt_pk_fp8_f32 v10, v0, v1
	v_mul_f32_e32 v0, v52, v35
	v_mul_f32_e32 v1, v52, v47
	v_mul_f32_e32 v3, v52, v58
	v_cvt_pk_fp8_f32 v11, v0, v1
	v_cvt_pk_fp8_f32 v8, v2, v3 op_sel:[0,0,1]
	v_mul_f32_e32 v2, v52, v56
	v_mul_f32_e32 v3, v52, v60
	v_cvt_pk_fp8_f32 v10, v2, v3 op_sel:[0,0,1]
	v_mul_f32_e32 v0, v52, v57
	v_mul_f32_e32 v1, v52, v61
	v_cvt_pk_fp8_f32 v11, v0, v1 op_sel:[0,0,1]
	ds_write2_b32 v51, v4, v8 offset0:24 offset1:28
	ds_write2_b32 v51, v5, v9 offset0:57 offset1:61
	ds_write2_b32 v51, v6, v10 offset0:90 offset1:94
	ds_write2_b32 v51, v7, v11 offset0:123 offset1:127
	s_waitcnt lgkmcnt(0)
	s_cbranch_vccnz .LBB0_116
	s_cmpk_gt_i32 s71, 0x57
	s_cselect_b32 s2, 0xffffea00, 0
	s_mul_i32 s3, s65, s70
	s_cselect_b32 s38, 0x80, 0
	s_sub_i32 s2, s2, s3
	s_add_i32 s2, s68, s2
	s_lshl_b32 s2, s2, 1
	s_and_b32 s3, s69, 64
	s_and_b32 s2, s2, 0xffffff00
	s_or_b32 s3, s3, s38
	s_or_b32 s69, s3, s2
	s_branch .LBB0_116
